# grid barrier: XCD leader issues its invalidate right after the release write-back and waits only for the write-back (vmcnt(1)) before the cross-XCD arrival atomic; members invalidate before they start
# baseline (speedup 1.0000x reference)
.LBB0_125:
	s_or_b64 exec, exec, s[6:7]
	v_cvt_f32_u32_e32 v5, v3
	s_waitcnt vmcnt(0)
	v_readfirstlane_b32 s4, v4
	v_sub_u32_e32 v4, 0, v3
	v_rcp_iflag_f32_e32 v5, v5
	v_add_u32_e32 v6, s4, v2
	v_mul_f32_e32 v5, 0x4f7ffffe, v5
	v_cvt_u32_f32_e32 v5, v5
	v_mul_lo_u32 v2, v4, v5
	v_mul_hi_u32 v2, v5, v2
	v_add_u32_e32 v2, v5, v2
	v_mul_hi_u32 v2, v6, v2
	v_mul_lo_u32 v4, v2, v3
	v_sub_u32_e32 v4, v6, v4
	v_add_u32_e32 v5, 1, v2
	v_cmp_ge_u32_e32 vcc, v4, v3
	s_nop 1
	v_cndmask_b32_e32 v2, v2, v5, vcc
	v_sub_u32_e32 v5, v4, v3
	v_cndmask_b32_e32 v4, v4, v5, vcc
	v_add_u32_e32 v5, 1, v2
	v_cmp_ge_u32_e32 vcc, v4, v3
	v_add_u32_e32 v4, 1, v6
	s_nop 0
	v_cndmask_b32_e32 v2, v2, v5, vcc
	v_mul_lo_u32 v5, v3, v2
	v_add_u32_e32 v3, v5, v3
	v_cmp_ne_u32_e32 vcc, v4, v3
	s_and_saveexec_b64 s[4:5], vcc
	s_xor_b64 s[4:5], exec, s[4:5]
	s_cbranch_execz .LBB0_139
	buffer_inv sc1
	s_movk_i32 s6, 0xd40
	s_mov_b32 s7, 0
	s_lshl_b64 s[6:7], s[6:7], 2
	s_add_u32 s8, s54, s6
	s_addc_u32 s9, s55, s7
	s_waitcnt lgkmcnt(0)
	v_mov_b32_e32 v1, 0
	global_load_dword v3, v1, s[8:9] sc1
	s_waitcnt vmcnt(0)
	v_cmp_eq_u32_e32 vcc, v3, v2
	s_and_saveexec_b64 s[6:7], vcc
	s_cbranch_execz .LBB0_138
	s_mov_b32 s20, 1
	s_mov_b64 s[10:11], 0
	s_branch .LBB0_129

.LBB0_139:
	s_andn2_saveexec_b64 s[4:5], s[4:5]
	s_cbranch_execz .LBB0_159
	s_mov_b64 s[4:5], exec
	buffer_wbl2 sc1
	buffer_inv sc1
	s_waitcnt lgkmcnt(0)
	s_waitcnt vmcnt(1)
	v_mbcnt_lo_u32_b32 v2, s4, 0
	v_mbcnt_hi_u32_b32 v2, s5, v2
	v_cmp_eq_u32_e32 vcc, 0, v2
	s_and_saveexec_b64 s[6:7], vcc
	s_cbranch_execz .LBB0_142
	s_bcnt1_i32_b64 s4, s[4:5]
	v_mov_b32_e32 v3, 0x3000
	v_mov_b32_e32 v4, s4
	global_atomic_add v3, v3, v4, s[54:55] offset:1024 sc0

.LBB0_224:
	s_or_b64 exec, exec, s[6:7]
	v_cvt_f32_u32_e32 v6, v4
	s_waitcnt vmcnt(0)
	v_readfirstlane_b32 s4, v5
	v_sub_u32_e32 v5, 0, v4
	v_rcp_iflag_f32_e32 v6, v6
	v_add_u32_e32 v7, s4, v3
	v_mul_f32_e32 v6, 0x4f7ffffe, v6
	v_cvt_u32_f32_e32 v6, v6
	v_mul_lo_u32 v3, v5, v6
	v_mul_hi_u32 v3, v6, v3
	v_add_u32_e32 v3, v6, v3
	v_mul_hi_u32 v3, v7, v3
	v_mul_lo_u32 v5, v3, v4
	v_sub_u32_e32 v5, v7, v5
	v_add_u32_e32 v6, 1, v3
	v_cmp_ge_u32_e32 vcc, v5, v4
	s_nop 1
	v_cndmask_b32_e32 v3, v3, v6, vcc
	v_sub_u32_e32 v6, v5, v4
	v_cndmask_b32_e32 v5, v5, v6, vcc
	v_add_u32_e32 v6, 1, v3
	v_cmp_ge_u32_e32 vcc, v5, v4
	v_add_u32_e32 v5, 1, v7
	s_nop 0
	v_cndmask_b32_e32 v3, v3, v6, vcc
	v_mul_lo_u32 v6, v4, v3
	v_add_u32_e32 v4, v6, v4
	v_cmp_ne_u32_e32 vcc, v5, v4
	s_and_saveexec_b64 s[4:5], vcc
	s_xor_b64 s[4:5], exec, s[4:5]
	s_cbranch_execz .LBB0_238
	buffer_inv sc1
	s_movk_i32 s6, 0xd40
	s_mov_b32 s7, s56
	s_lshl_b64 s[6:7], s[6:7], 2
	s_add_u32 s8, s54, s6
	s_addc_u32 s9, s55, s7
	s_waitcnt lgkmcnt(0)
	global_load_dword v2, v227, s[8:9] sc1
	s_waitcnt vmcnt(0)
	v_cmp_eq_u32_e32 vcc, v2, v3
	s_and_saveexec_b64 s[6:7], vcc
	s_cbranch_execz .LBB0_237
	s_mov_b32 s21, 1
	s_mov_b64 s[10:11], 0
	s_branch .LBB0_228

.LBB0_238:
	s_andn2_saveexec_b64 s[4:5], s[4:5]
	s_cbranch_execz .LBB0_258
	s_mov_b64 s[4:5], exec
	buffer_wbl2 sc1
	buffer_inv sc1
	s_waitcnt lgkmcnt(0)
	s_waitcnt vmcnt(1)
	v_mbcnt_lo_u32_b32 v3, s4, 0
	v_mbcnt_hi_u32_b32 v3, s5, v3
	v_cmp_eq_u32_e32 vcc, 0, v3
	s_and_saveexec_b64 s[6:7], vcc
	s_cbranch_execz .LBB0_241
	s_bcnt1_i32_b64 s4, s[4:5]
	v_mov_b32_e32 v4, s4
	v_readlane_b32 s4, v255, 2
	v_readlane_b32 s5, v255, 3
	s_nop 4
	global_atomic_add v4, v227, v4, s[4:5] sc0

.LBB0_1365:
	s_mov_b64 s[4:5], exec
	buffer_wbl2 sc1
	buffer_inv sc1
	s_waitcnt lgkmcnt(0)
	s_waitcnt vmcnt(1)
	v_mbcnt_lo_u32_b32 v3, s4, 0
	v_mbcnt_hi_u32_b32 v3, s5, v3
	v_cmp_eq_u32_e32 vcc, 0, v3
	s_and_saveexec_b64 s[6:7], vcc
	s_cbranch_execz .LBB0_1367
	s_bcnt1_i32_b64 s4, s[4:5]
	v_mov_b32_e32 v4, s4
	v_readlane_b32 s4, v255, 2
	v_readlane_b32 s5, v255, 3
	s_nop 4
	global_atomic_add v4, v227, v4, s[4:5] sc0
